# speedup vs baseline: 1.0036x; 1.0036x over previous
_Z5k2_kvPKDF16_S0_S0_S0_PDF16_S1_Pf:
	s_load_dwordx8 s[12:19], s[0:1], 0x0
	s_lshl_b32 s3, s2, 1
	s_and_b32 s3, s3, 14
	s_bfe_u32 s25, s2, 0x10006
	v_bfe_u32 v4, v0, 6, 2
	v_and_b32_e32 v1, 15, v0
	s_or_b32 s5, s3, s25
	v_mul_u32_u24_e32 v4, 48, v4
	s_lshl_b32 s24, s5, 3
	s_movk_i32 s5, 0x100
	v_or_b32_e32 v47, v4, v1
	s_bfe_u32 s3, s2, 0x30003
	s_waitcnt lgkmcnt(0)
	v_mov_b32_e32 v2, s15
	v_mov_b32_e32 v3, s13
	v_cmp_gt_u32_e64 s[10:11], s5, v0
	v_mul_lo_u16_e32 v4, 57, v47
	s_lshl_b32 s26, s3, 4
	v_cndmask_b32_e64 v3, v2, v3, s[10:11]
	v_mov_b32_e32 v2, s14
	v_mov_b32_e32 v5, s12
	s_add_i32 s5, s24, -1
	v_lshrrev_b16_e32 v4, 10, v4
	v_cndmask_b32_e64 v2, v2, v5, s[10:11]
	s_add_i32 s6, s26, -1
	v_mul_i32_i24_e32 v5, 0xffffffee, v4
	v_add_u32_e32 v55, s5, v4
	s_lshr_b32 s4, s2, 7
	v_add3_u32 v57, s6, v47, v5
	v_max_i32_e32 v4, 0, v55
	v_mov_b32_e32 v6, 0x7f
	v_bfe_u32 v46, v0, 4, 2
	s_lshl_b32 s7, s4, 14
	v_med3_i32 v5, v57, 0, v6
	v_lshlrev_b32_e32 v4, 7, v4
	v_lshlrev_b32_e32 v48, 3, v46
	v_or3_b32 v4, v4, v5, s7
	v_lshl_or_b32 v42, v4, 6, v48
	v_mov_b32_e32 v43, 0
	v_lshl_add_u64 v[4:5], v[42:43], 1, v[2:3]
	v_add_u32_e32 v49, 16, v47
	v_mov_b32_e32 v7, 57
	global_load_dwordx4 v[18:21], v[4:5], off
	global_load_dwordx4 v[22:25], v[4:5], off offset:64
	v_mul_lo_u16_sdwa v4, v49, v7 dst_sel:DWORD dst_unused:UNUSED_PAD src0_sel:BYTE_0 src1_sel:DWORD
	v_lshrrev_b16_e32 v4, 10, v4
	v_mul_i32_i24_e32 v5, 0xffffffee, v4
	v_add_u32_e32 v74, s5, v4
	v_add3_u32 v75, s6, v49, v5
	v_med3_i32 v4, v74, 0, v6
	v_med3_i32 v5, v75, 0, v6
	v_lshlrev_b32_e32 v4, 7, v4
	v_or3_b32 v4, v4, v5, s7
	v_lshl_or_b32 v42, v4, 6, v48
	v_lshl_add_u64 v[4:5], v[42:43], 1, v[2:3]
	v_add_u32_e32 v51, 32, v47
	global_load_dwordx4 v[26:29], v[4:5], off
	global_load_dwordx4 v[30:33], v[4:5], off offset:64
	v_mul_lo_u16_sdwa v4, v51, v7 dst_sel:DWORD dst_unused:UNUSED_PAD src0_sel:BYTE_0 src1_sel:DWORD
	v_lshrrev_b16_e32 v4, 10, v4
	v_mul_i32_i24_e32 v5, 0xffffffee, v4
	v_add_u32_e32 v54, s5, v4
	v_add3_u32 v56, s6, v51, v5
	v_min_u32_e32 v4, 0x7f, v54
	v_med3_i32 v5, v56, 0, v6
	v_lshlrev_b32_e32 v4, 7, v4
	v_or3_b32 v4, v4, v5, s7
	v_lshl_or_b32 v42, v4, 6, v48
	v_lshl_add_u64 v[2:3], v[42:43], 1, v[2:3]
	global_load_dwordx4 v[34:37], v[2:3], off
	global_load_dwordx4 v[38:41], v[2:3], off offset:64
	v_lshrrev_b32_e32 v52, 8, v0
	v_lshlrev_b32_e32 v2, 7, v1
	v_lshl_or_b32 v42, v52, 14, v2
	v_lshl_add_u64 v[2:3], s[18:19], 0, v[42:43]
	v_lshlrev_b32_e32 v44, 4, v46
	v_mov_b32_e32 v45, v43
	v_lshl_add_u64 v[78:79], v[2:3], 0, v[44:45]
	v_bfe_u32 v45, v0, 7, 1
	v_bfe_u32 v50, v0, 6, 1
	s_lshl_b32 s5, s4, 6
	v_lshlrev_b32_e32 v3, 4, v45
	v_lshl_or_b32 v2, v50, 6, v48
	v_or3_b32 v10, v3, s5, v1
	s_lshl_b32 s5, s3, 5
	s_add_u32 s6, s16, s5
	v_lshrrev_b32_e32 v2, 4, v2
	v_mov_b32_e32 v11, v43
	s_addc_u32 s7, s17, 0
	v_and_b32_e32 v42, 16, v0
	v_or_b32_e32 v4, s24, v2
	v_lshlrev_b64 v[2:3], 15, v[10:11]
	v_or_b32_e32 v10, 32, v10
	v_lshl_add_u64 v[12:13], s[6:7], 0, v[42:43]
	v_lshlrev_b32_e32 v14, 8, v4
	v_lshlrev_b64 v[10:11], 15, v[10:11]
	s_mov_b64 s[28:29], 0x2000
	v_lshl_add_u64 v[78:79], v[78:79], 0, s[28:29]
	global_load_dwordx4 v[66:69], v[78:79], off
	global_load_dwordx4 v[70:73], v[78:79], off offset:64
	global_load_dwordx4 v[58:61], v[78:79], off offset:2048
	global_load_dwordx4 v[62:65], v[78:79], off offset:2112
	v_lshl_add_u64 v[2:3], v[12:13], 0, v[2:3]
	v_mov_b32_e32 v15, v43
	v_or_b32_e32 v16, 0x200, v14
	v_mov_b32_e32 v17, v43
	v_lshl_add_u64 v[10:11], v[12:13], 0, v[10:11]
	v_lshl_add_u64 v[4:5], v[2:3], 0, v[14:15]
	v_lshl_add_u64 v[6:7], v[2:3], 0, v[16:17]
	v_lshl_add_u64 v[12:13], v[10:11], 0, v[14:15]
	v_lshl_add_u64 v[14:15], v[10:11], 0, v[16:17]
	global_load_dwordx4 v[2:5], v[4:5], off
	s_nop 0
	global_load_dwordx4 v[6:9], v[6:7], off
	s_nop 0
	global_load_dwordx4 v[10:13], v[12:13], off
	s_nop 0
	global_load_dwordx4 v[14:17], v[14:15], off
	s_load_dwordx4 s[20:23], s[0:1], 0x20
	s_load_dwordx2 s[16:17], s[0:1], 0x30
	s_movk_i32 s0, 0x90
	v_lshrrev_b32_e32 v53, 6, v0
	s_mov_b32 s12, 0
	v_cmp_gt_u32_e32 vcc, s0, v0
	s_and_saveexec_b64 s[0:1], vcc
	s_cbranch_execz .LBB2_2
	v_lshlrev_b32_e32 v76, 4, v0
	v_mov_b32_e32 v77, v43
	v_lshl_add_u64 v[80:81], s[18:19], 0, v[76:77]
	v_add_co_u32_e32 v80, vcc, 0x8000, v80
	v_add_u32_e32 v76, 0x10e00, v76
	s_nop 0
	v_addc_co_u32_e32 v81, vcc, 0, v81, vcc
	global_load_dwordx4 v[80:83], v[80:81], off
	s_waitcnt vmcnt(0)
	ds_write_b128 v76, v[80:83]
.LBB2_2:
	s_or_b64 exec, exec, s[0:1]
	v_or_b32_e32 v55, v57, v55
	s_movk_i32 s0, 0x80
	v_cmp_gt_u32_e32 vcc, s0, v55
	v_or_b32_e32 v55, v75, v74
	s_movk_i32 s1, 0xb4
	s_waitcnt vmcnt(13)
	v_cndmask_b32_e32 v21, 0, v21, vcc
	v_cndmask_b32_e32 v20, 0, v20, vcc
	v_cndmask_b32_e32 v19, 0, v19, vcc
	v_cndmask_b32_e32 v18, 0, v18, vcc
	s_waitcnt vmcnt(12)
	v_cndmask_b32_e32 v25, 0, v25, vcc
	v_cndmask_b32_e32 v24, 0, v24, vcc
	v_cndmask_b32_e32 v23, 0, v23, vcc
	v_cndmask_b32_e32 v22, 0, v22, vcc
	v_cmp_gt_u32_e32 vcc, s0, v55
	v_or_b32_e32 v54, v56, v54
	v_lshrrev_b32_e32 v55, 2, v1
	s_waitcnt vmcnt(11)
	v_cndmask_b32_e32 v29, 0, v29, vcc
	v_cndmask_b32_e32 v28, 0, v28, vcc
	v_cndmask_b32_e32 v27, 0, v27, vcc
	v_cndmask_b32_e32 v26, 0, v26, vcc
	s_waitcnt vmcnt(10)
	v_cndmask_b32_e32 v33, 0, v33, vcc
	v_cndmask_b32_e32 v32, 0, v32, vcc
	v_cndmask_b32_e32 v31, 0, v31, vcc
	v_cndmask_b32_e32 v30, 0, v30, vcc
	v_cmp_gt_u32_e32 vcc, s1, v51
	v_cmp_gt_u32_e64 s[0:1], s0, v54
	s_and_b64 vcc, vcc, s[0:1]
	s_waitcnt vmcnt(9)
	v_cndmask_b32_e32 v37, 0, v37, vcc
	v_cndmask_b32_e32 v36, 0, v36, vcc
	v_cndmask_b32_e32 v35, 0, v35, vcc
	v_cndmask_b32_e32 v34, 0, v34, vcc
	s_waitcnt vmcnt(8)
	v_cndmask_b32_e32 v41, 0, v41, vcc
	v_cndmask_b32_e32 v40, 0, v40, vcc
	v_cndmask_b32_e32 v39, 0, v39, vcc
	v_cndmask_b32_e32 v38, 0, v38, vcc
	v_cmp_ne_u32_e32 vcc, 0, v42
	v_or_b32_e32 v75, v48, v55
	v_and_b32_e32 v56, 3, v0
	v_cndmask_b32_e64 v42, 0, 3, vcc
	v_add_u32_e32 v42, v42, v0
	v_and_b32_e32 v42, 15, v42
	v_mul_u32_u24_e32 v57, 0x3c00, v52
	v_mul_u32_u24_e32 v74, 0x2800, v52
	v_mul_u32_u24_e32 v75, 0x50, v75
	v_lshlrev_b32_e32 v76, 5, v45
	s_mov_b32 s5, s12
	s_movk_i32 s13, 0x50
	v_add3_u32 v74, v74, v75, v76
	v_lshlrev_b32_e32 v75, 3, v56
	v_or_b32_e32 v57, v57, v48
	v_mad_u32_u24 v48, v53, 18, v42
	s_lshl_b64 s[14:15], s[4:5], 14
	v_cmp_ne_u32_e64 s[4:5], 0, v56
	v_cmp_ne_u32_e64 s[6:7], 1, v56
	v_cmp_eq_u32_e64 s[8:9], 2, v56
	v_mul_u32_u24_e32 v56, 0x50, v49
	v_mov_b32_e32 v49, 0x5a0
	v_mad_u32_u24 v93, v48, s13, v49
	v_mov_b32_e32 v49, 0xa0
	v_mad_u32_u24 v92, v48, s13, v49
	v_mov_b32_e32 v49, 0x5f0
	v_mad_u32_u24 v94, v48, s13, v49
	v_mov_b32_e32 v49, 0x640
	v_mad_u32_u24 v95, v48, s13, v49
	v_mov_b32_e32 v49, 0xb40
	v_mad_u32_u24 v96, v48, s13, v49
	v_mov_b32_e32 v49, 0xb90
	s_movk_i32 s0, 0x7800
	s_movk_i32 s18, 0x2300
	v_lshlrev_b32_e32 v52, 12, v52
	v_mad_u32_u24 v97, v48, s13, v49
	v_mov_b32_e32 v49, 0xbe0
	v_lshl_or_b32 v54, v53, 4, v42
	v_add3_u32 v74, v74, v75, s0
	v_mov_b32_e32 v75, 0x7800
	v_lshlrev_b32_e32 v76, 8, v46
	v_mul_u32_u24_e32 v77, 0x50, v48
	v_mad_u32_u24 v91, v48, s13, s13
	v_mad_u32_u24 v98, v48, s13, v49
	v_mad_u32_u24 v48, v50, s18, v52
	v_lshlrev_b32_e32 v49, 10, v45
	v_mad_u32_u24 v54, v54, s13, v75
	v_mul_u32_u24_e32 v75, 0x2300, v50
	v_add3_u32 v48, v48, v49, v76
	v_lshlrev_b32_e32 v49, 2, v1
	v_lshlrev_b32_e32 v45, 6, v45
	v_cmp_eq_u32_e64 s[0:1], v55, v46
	v_and_b32_e32 v55, 0x100, v0
	v_or3_b32 v45, v75, v45, v49
	s_mov_b32 s13, 0xe900
	v_add3_u32 v84, v45, v55, s13
	v_add_u32_e32 v85, 0xe800, v45
	s_and_b32 s13, s2, 7
	v_lshlrev_b32_e32 v45, 7, v53
	v_lshl_or_b32 v45, s13, 11, v45
	v_lshl_or_b32 v45, s25, 10, v45
	v_or_b32_e32 v45, s14, v45
	v_or_b32_e32 v1, v48, v49
	v_mov_b32_e32 v49, s15
	v_or_b32_e32 v48, s26, v45
	v_lshl_add_u64 v[42:43], v[48:49], 0, v[42:43]
	v_lshlrev_b64 v[42:43], 7, v[42:43]
	s_mov_b32 s14, 0
	s_waitcnt lgkmcnt(0)
	s_barrier
	v_and_or_b32 v42, v0, 48, v42
	s_mov_b32 s15, 0
	v_mul_u32_u24_e32 v47, 0x50, v47
	v_mul_u32_u24_e32 v51, 0x50, v51
	v_mul_u32_u24_e32 v100, 0x1400, v50
	v_lshl_add_u64 v[42:43], v[42:43], 0, s[14:15]
	v_add_u32_e32 v1, 0xc800, v1
	s_waitcnt lgkmcnt(0)
	v_lshl_add_u64 v[80:81], s[22:23], 0, v[42:43]
	v_lshl_add_u64 v[82:83], s[20:21], 0, v[42:43]
	v_mul_u32_u24_e32 v86, 0x90, v46
	s_mov_b64 s[18:19], 0
	v_add_u32_e32 v87, v57, v47
	v_add_u32_e32 v88, v57, v56
	v_add_u32_e32 v89, v57, v51
	v_add_u32_e32 v90, v77, v44
	v_add_u32_e32 v91, v91, v44
	v_add_u32_e32 v92, v92, v44
	v_add_u32_e32 v93, v93, v44
	v_add_u32_e32 v94, v94, v44
	v_add_u32_e32 v95, v95, v44
	v_add_u32_e32 v96, v96, v44
	v_add_u32_e32 v97, v97, v44
	v_add_u32_e32 v98, v98, v44
	v_add_u32_e32 v99, v54, v44
	v_add_u32_e32 v100, v74, v100
	v_add_u32_e32 v1, 0xfffff000, v1
	v_add_u32_e32 v84, 0xffffff00, v84
	v_add_u32_e32 v85, 0xffffff00, v85
	v_add_u32_e32 v86, 0x480, v86
	s_mov_b32 s25, 2
	s_branch .LBB2_7

.LBB2_6:
	s_add_i32 s25, s25, 1
	s_and_b32 s25, s25, 3
	s_add_u32 s18, s18, 0x1000
	s_addc_u32 s19, s19, 0
	v_add_u32_e32 v1, 0x800, v1
	v_add_u32_e32 v84, 0x80, v84
	v_add_u32_e32 v85, 0x80, v85
	v_lshl_add_u64 v[80:81], v[80:81], 0, 64
	v_lshl_add_u64 v[82:83], v[82:83], 0, 64
	s_movk_i32 s28, 0x240
	s_cmp_eq_u32 s25, 0
	s_cselect_b32 s28, 0xfffff940, s28
	v_add_u32_e32 v86, s28, v86
	s_cmpk_eq_i32 s18, 0x4000
	s_waitcnt vmcnt(3)
	v_mov_b32_e32 v66, v42
	v_mov_b32_e32 v67, v43
	v_mov_b32_e32 v68, v44
	v_mov_b32_e32 v69, v45
	s_waitcnt vmcnt(2)
	v_mov_b32_e32 v70, v46
	v_mov_b32_e32 v71, v47
	v_mov_b32_e32 v72, v48
	v_mov_b32_e32 v73, v49
	s_waitcnt vmcnt(1)
	v_mov_b32_e32 v58, v50
	v_mov_b32_e32 v59, v51
	v_mov_b32_e32 v60, v52
	v_mov_b32_e32 v61, v53
	s_waitcnt vmcnt(0)
	v_mov_b32_e32 v62, v54
	v_mov_b32_e32 v63, v55
	v_mov_b32_e32 v64, v56
	v_mov_b32_e32 v65, v57
	s_cbranch_scc1 .LBB2_28
.LBB2_7:
	s_cmpk_eq_i32 s18, 0x3000
	s_cbranch_scc1 .LBB2_9
	s_mov_b32 s28, 0xffffe000
	s_cmp_eq_u32 s25, 3
	s_cselect_b32 s28, 0xffffd000, s28
	s_cmp_eq_u32 s25, 2
	s_cselect_b32 s28, 0, s28
	s_ashr_i32 s29, s28, 31
	v_lshl_add_u64 v[42:43], v[78:79], 0, s[28:29]
	v_add_co_u32_e32 v54, vcc, 0x1000, v42
	s_nop 1
	v_addc_co_u32_e32 v55, vcc, 0, v43, vcc
	global_load_dwordx4 v[42:45], v[54:55], off
	global_load_dwordx4 v[46:49], v[54:55], off offset:64
	global_load_dwordx4 v[50:53], v[54:55], off offset:2048
	s_nop 0
	global_load_dwordx4 v[54:57], v[54:55], off offset:2112
	s_branch .LBB2_10

.LBB2_14:
	s_waitcnt lgkmcnt(0)
	s_barrier
	s_andn2_b64 vcc, exec, s[14:15]
	s_cbranch_vccnz .LBB2_6
	s_cmp_eq_u32 s25, 0
	s_cselect_b64 vcc, -1, 0
	s_waitcnt vmcnt(1)
	v_cndmask_b32_e32 v69, v13, v5, vcc
	v_cndmask_b32_e32 v68, v12, v4, vcc
	v_cndmask_b32_e32 v67, v11, v3, vcc
	v_cndmask_b32_e32 v66, v10, v2, vcc
	ds_read_b64_tr_b16 v[70:71], v100
	ds_read_b64_tr_b16 v[72:73], v100 offset:320
	s_waitcnt lgkmcnt(0)
	v_mfma_f32_16x16x32_f16 v[62:65], v[66:69], v[70:73], 0
	s_mov_b32 s14, s12
	s_mov_b32 s15, s12
	s_mov_b32 s13, s12
	v_mfma_f32_16x16x32_f16 v[70:73], v[70:73], v[70:73], 0
	v_mov_b64_e32 v[60:61], s[14:15]
	v_mov_b64_e32 v[58:59], s[12:13]
	s_and_saveexec_b64 s[14:15], s[10:11]
	v_mfma_f32_16x16x32_f16 v[58:61], v[66:69], v[66:69], 0
	s_or_b64 exec, exec, s[14:15]
	s_waitcnt vmcnt(0)
	v_cndmask_b32_e32 v69, v17, v9, vcc
	v_cndmask_b32_e32 v68, v16, v8, vcc
	v_cndmask_b32_e32 v67, v15, v7, vcc
	v_cndmask_b32_e32 v66, v14, v6, vcc
	ds_read_b64_tr_b16 v[102:103], v100 offset:2560
	ds_read_b64_tr_b16 v[104:105], v100 offset:2880
	s_waitcnt lgkmcnt(0)
	v_mfma_f32_16x16x32_f16 v[74:77], v[66:69], v[102:105], v[62:65]
	v_mfma_f32_16x16x32_f16 v[62:65], v[102:105], v[102:105], v[70:73]
	s_and_saveexec_b64 s[14:15], s[10:11]
	v_mfma_f32_16x16x32_f16 v[58:61], v[66:69], v[66:69], v[58:61]
	s_or_b64 exec, exec, s[14:15]
	s_nop 3
	ds_write2_b32 v1, v74, v75 offset1:16
	ds_write2_b32 v1, v76, v77 offset0:32 offset1:48
	s_and_saveexec_b64 s[14:15], s[0:1]
	s_cbranch_execz .LBB2_5
	s_and_saveexec_b64 s[20:21], s[4:5]
	s_xor_b64 s[20:21], exec, s[20:21]
	s_cbranch_execz .LBB2_24
	v_mov_b32_e32 v62, v63
	s_and_saveexec_b64 s[22:23], s[6:7]
	s_xor_b64 s[22:23], exec, s[22:23]
	v_cndmask_b32_e64 v62, v65, v64, s[8:9]
	s_andn2_saveexec_b64 s[22:23], s[22:23]
	s_or_b64 exec, exec, s[22:23]
